# v72 without the wave 4-7 start delay in the weight-copy chunks
# baseline (speedup 1.0000x reference)
.LBB6_901:
	s_lshl_b32 s84, s0, 3
	s_or_b32 s1, s84, s59
	s_lshl_b32 s2, s1, 1
	s_add_i32 s3, s1, 0x100
	s_cmp_lt_u32 s1, 0x100
	s_cselect_b32 s2, s2, s3
	s_mul_i32 s2, s63, s2
	s_lshr_b32 s2, s2, 10
	s_and_b32 s90, s2, 0xffffffe0
	s_add_i32 s1, s1, 1
	s_lshl_b32 s2, s1, 1
	s_add_i32 s3, s1, 0x100
	s_cmp_lt_u32 s1, 0x100
	s_cselect_b32 s2, s2, s3
	s_mul_i32 s2, s63, s2
	s_lshr_b32 s2, s2, 10
	s_and_b32 s91, s2, 0xffffffe0
	s_bitcmp0_b32 s0, 0
	s_cselect_b64 s[22:23], -1, 0
	s_and_b64 vcc, exec, s[22:23]
	s_cbranch_vccnz .LBB6_1210
	v_readlane_b32 s6, v254, 13
	v_readlane_b32 s7, v254, 14
	s_waitcnt vmcnt(0)
	v_mov_b32_e32 v167, v0
	s_max_i32 s64, s90, 0
	v_readfirstlane_b32 s0, v167
	s_ashr_i32 s95, s0, 6
	v_readlane_b32 s0, v254, 60
	s_lshl_b32 s81, s95, 14
	v_readlane_b32 s1, v254, 61
	v_and_b32_e32 v166, 63, v167
	s_add_i32 s94, s81, 0
	s_mov_b64 s[2:3], -1
	s_and_b64 vcc, exec, s[0:1]
	s_cbranch_vccz .LBB6_915
	s_min_i32 s30, s91, 0xdc00
	s_cmp_le_i32 s30, s64
	s_cbranch_scc1 .LBB6_908
	s_sub_i32 s0, s30, s64
	s_mov_b32 s2, 18
	s_cmp_lt_i32 s0, 32
	s_cbranch_scc1 .LBB6_908
	s_add_i32 s31, s95, s64
	s_cmp_ge_i32 s31, s30
	s_cbranch_scc1 .LBB6_908
	s_ashr_i32 s3, s2, 31
	s_lshl_b64 s[0:1], s[2:3], 3
	s_add_u32 s0, s76, s0
	s_addc_u32 s1, s77, s1
	s_load_dwordx2 s[0:1], s[0:1], 0x0
	v_lshrrev_b32_e32 v4, 3, v166
	v_lshlrev_b32_e32 v2, 2, v166
	v_mul_u32_u24_e32 v5, 0x2c00, v4
	v_and_b32_e32 v6, 28, v2
	s_waitcnt lgkmcnt(0)
	s_add_u32 s34, s0, 0x10800000
	v_or_b32_e32 v2, v5, v6
	v_lshl_add_u32 v5, v6, 2, s94
	v_lshlrev_b32_e32 v6, 5, v166
	s_addc_u32 s35, s1, 0
	v_lshrrev_b32_e32 v135, 2, v166
	v_lshlrev_b32_e32 v132, 4, v166
	v_and_b32_e32 v132, 48, v132
	s_add_u32 s36, s6, 0x85280000
	v_mul_u32_u24_e32 v4, 0x84, v4
	v_mul_u32_u24_e32 v6, 0x84, v132
	v_lshlrev_b32_e32 v7, 2, v135
	v_and_b32_e32 v134, 31, v167
	s_addc_u32 s37, s7, 0
	v_lshlrev_b32_e32 v2, 2, v2
	v_add3_u32 v136, s94, v6, v7
	v_mov_b32_e32 v133, v3
	v_add_u32_e32 v137, v5, v4
